# v12: plus LDS wait consolidation in MLA loop (one lgkmcnt(0) at PV start, drain for waves 4-7 at iteration end)
# baseline (speedup 1.0000x reference)
; #define SFENCE() __builtin_amdgcn_sched_barrier(0)
; template <bool FOX>
; __device__ __forceinline__ void attn_unit(const Args& A, int b, int h, int qb, LAS char* shm, LAS float* dg) {
;     ...
;         { if constexpr (!FOX) { if (t0 + t == tw_last + 1) {
; #pragma unroll
;                   for (int r = 0; r < 16; ++r) negm[r] = -INFINITY;
;                   asm volatile("" : "+v"(negm)); } }
;           const lds_cptr vp = vp0 + ((t - 1) % NS) * VSLOT; float sa = 0.f, sb = 0.f;
; #pragma unroll
;           for (int g = 0; g < 2 * NQ; ++g) {
;               if (!FOX && g == 0) c0 = __builtin_amdgcn_mfma_f32_32x32x16_bf16(kf[0], qr[0], negm, 0, 0, 0);
;               else if (!FOX && g == 1) c1 = __builtin_amdgcn_mfma_f32_32x32x16_bf16(kf[1], qr[0], negm, 0, 0, 0);
;               else if (g & 1) c1 = __builtin_amdgcn_mfma_f32_32x32x16_bf16(kf[g], qr[g >> 1], c1, 0, 0, 0); else c0 = __builtin_amdgcn_mfma_f32_32x32x16_bf16(kf[g], qr[g >> 1], c0, 0, 0, 0);
;               if (g < 8) { const int i = (g >> 1) + 4 * (g & 1); vlo[i] = vtr(vp + (i >> 2) * 4096 + (i & 3) * 1024); vhi[i] = vtr(vp + (i >> 2) * 4096 + (i & 3) * 1024 + 512);
;                   if (g < 4) { sa += pp0[4 * g]; sb += pp0[4 * g + 1]; sa += pp0[4 * g + 2]; sb += pp0[4 * g + 3]; } else { sa += pp1[4 * g - 16]; sb += pp1[4 * g - 15]; sa += pp1[4 * g - 14]; sb += pp1[4 * g - 13]; }
;                   asm volatile("" : "+v"(sa), "+v"(sb)); }
;               { constexpr int G0 = FOX ? 0 : 4; if (g >= G0) { const int q = 2 * (g - G0);
; #pragma unroll
;                   for (int k = 0; k < 2; ++k) { const int w = q + k; const unsigned pkd = w < 8 ? cvt_pk_bf16(pp0[2 * w], pp0[2 * w + 1]) : cvt_pk_bf16(pp1[2 * w - 16], pp1[2 * w - 15]); pw[w >> 2][w & 3] = pkd; } } }
;               SFENCE();
;           }
;           lrun += sa + sb; }
;         MASKONLY(t);
;         float rm; ROWMAX(rm);
;         bool resc = false;
;         if (__any(rm > THR)) { const float dl = fmaxf(rm, 0.f); mhat += dl;
; #pragma unroll
;             for (int r = 0; r < 16; ++r) { c0[r] -= dl; c1[r] -= dl; }
;             if constexpr (!FOX) {
; #pragma unroll
;                 for (int r = 0; r < 16; ++r) negm[r] = -mhat;
;                 asm volatile("" : "+v"(negm)); }
;             const float f = __builtin_amdgcn_exp2f(-dl); lrun *= f; if (hi == 0) wsf[r32] = f; resc = true; }
.LBB0_835:
	s_add_i32 s27, s42, 0x8000
	v_mfma_f32_32x32x16_bf16 v[114:129], v[206:209], v[138:141], v[82:97]
	s_and_b32 s27, s27, 0x6000
	v_add_u32_e32 v3, s27, v247
	ds_read_b64_tr_b16 v[206:207], v3 offset:49152
	ds_read_b64_tr_b16 v[208:209], v3 offset:49664
	v_add_f32_e32 v4, 0, v67
	v_add_f32_e32 v5, 0, v66
	v_add_f32_e32 v4, v69, v4
	v_add_f32_e32 v5, v68, v5
	v_mfma_f32_32x32x16_bf16 v[98:113], v[194:197], v[138:141], v[82:97]
	ds_read_b64_tr_b16 v[194:195], v3 offset:53248
	ds_read_b64_tr_b16 v[196:197], v3 offset:53760
	v_add_f32_e32 v4, v71, v4
	v_add_f32_e32 v5, v70, v5
	v_add_f32_e32 v4, v73, v4
	v_add_f32_e32 v5, v72, v5
	v_mfma_f32_32x32x16_bf16 v[114:129], v[202:205], v[142:145], v[114:129]
	ds_read_b64_tr_b16 v[202:203], v3 offset:50176
	ds_read_b64_tr_b16 v[204:205], v3 offset:50688
	v_add_f32_e32 v4, v75, v4
	v_add_f32_e32 v5, v74, v5
	v_add_f32_e32 v4, v77, v4
	v_add_f32_e32 v5, v76, v5
	v_mfma_f32_32x32x16_bf16 v[98:113], v[186:189], v[142:145], v[98:113]
	ds_read_b64_tr_b16 v[214:215], v3 offset:54272
	ds_read_b64_tr_b16 v[216:217], v3 offset:54784
	v_add_f32_e32 v4, v79, v4
	v_add_f32_e32 v5, v78, v5
	v_add_f32_e32 v4, v81, v4
	v_add_f32_e32 v5, v80, v5
	v_mfma_f32_32x32x16_bf16 v[114:129], v[198:201], v[146:149], v[114:129]
	ds_read_b64_tr_b16 v[210:211], v3 offset:51200
	ds_read_b64_tr_b16 v[212:213], v3 offset:51712
	v_add_f32_e32 v4, v51, v4
	v_add_f32_e32 v5, v50, v5
	v_add_f32_e32 v4, v53, v4
	v_add_f32_e32 v5, v52, v5
	v_cvt_pk_bf16_f32 v186, v66, v67
	v_cvt_pk_bf16_f32 v187, v68, v69
	v_mfma_f32_32x32x16_bf16 v[98:113], v[182:185], v[146:149], v[98:113]
	ds_read_b64_tr_b16 v[12:13], v3 offset:55296
	ds_read_b64_tr_b16 v[14:15], v3 offset:55808
	v_add_f32_e32 v4, v55, v4
	v_add_f32_e32 v5, v54, v5
	v_add_f32_e32 v4, v57, v4
	v_add_f32_e32 v5, v56, v5
	v_cvt_pk_bf16_f32 v188, v70, v71
	v_cvt_pk_bf16_f32 v189, v72, v73
	v_mfma_f32_32x32x16_bf16 v[114:129], v[190:193], v[150:153], v[114:129]
	ds_read_b64_tr_b16 v[8:9], v3 offset:52224
	ds_read_b64_tr_b16 v[10:11], v3 offset:52736
	v_add_f32_e32 v4, v59, v4
	v_add_f32_e32 v16, v61, v4
	v_add_f32_e32 v4, v58, v5
	v_add_f32_e32 v17, v60, v4
	v_cvt_pk_bf16_f32 v182, v74, v75
	v_cvt_pk_bf16_f32 v183, v76, v77
	v_mfma_f32_32x32x16_bf16 v[98:113], v[170:173], v[150:153], v[98:113]
	ds_read_b64_tr_b16 v[4:5], v3 offset:56320
	ds_read_b64_tr_b16 v[6:7], v3 offset:56832
	v_add_f32_e32 v3, v63, v16
	v_add_f32_e32 v16, v62, v17
	v_add_f32_e32 v3, v65, v3
	v_add_f32_e32 v16, v64, v16
	v_cvt_pk_bf16_f32 v184, v78, v79
	v_cvt_pk_bf16_f32 v185, v80, v81
	v_mfma_f32_32x32x16_bf16 v[114:129], v[178:181], v[154:157], v[114:129]
	v_cvt_pk_bf16_f32 v178, v50, v51
	v_cvt_pk_bf16_f32 v179, v52, v53
	v_mfma_f32_32x32x16_bf16 v[98:113], v[166:169], v[154:157], v[98:113]
	v_cvt_pk_bf16_f32 v180, v54, v55
	v_cvt_pk_bf16_f32 v181, v56, v57
	v_mfma_f32_32x32x16_bf16 v[114:129], v[174:177], v[158:161], v[114:129]
	v_cvt_pk_bf16_f32 v218, v58, v59
	v_cvt_pk_bf16_f32 v219, v60, v61
	v_mfma_f32_32x32x16_bf16 v[98:113], v[162:165], v[158:161], v[98:113]
	v_cvt_pk_bf16_f32 v220, v62, v63
	v_cvt_pk_bf16_f32 v221, v64, v65
	v_add_f32_e32 v3, v3, v16
	s_cmp_lg_u32 s98, 0
	s_cbranch_scc1 .Lmla_fixed_ref
	s_nop 9
	v_max_f32_e32 v16, v115, v115
	v_max_f32_e32 v17, v114, v114
	v_max_f32_e32 v16, v17, v16
	v_max3_f32 v17, v116, v117, v99
	v_max3_f32 v16, v16, v98, v100
	v_max3_f32 v16, v16, v101, v118
	v_max3_f32 v17, v17, v120, v121
	v_max3_f32 v16, v16, v119, v102
	v_max3_f32 v17, v17, v104, v105
	v_max3_f32 v16, v16, v103, v122
	v_max3_f32 v17, v17, v124, v125
	v_max3_f32 v16, v16, v123, v106
	v_max3_f32 v17, v17, v108, v109
	v_max3_f32 v16, v16, v107, v126
	v_max3_f32 v17, v17, v128, v129
	v_max3_f32 v16, v16, v127, v110
	v_max3_f32 v17, v17, v112, v113
	v_add_f32_e32 v246, v246, v3
	v_max3_f32 v3, v16, v111, v17
	v_mov_b32_e32 v16, v3
	s_nop 1
	v_permlane32_swap_b32_e32 v3, v16
	v_max_f32_e32 v16, v16, v16
	v_max_f32_e32 v3, v3, v3
	v_max_f32_e32 v3, v3, v16
	v_cmp_lt_f32_e32 vcc, s95, v3
	s_cmp_lg_u64 vcc, 0
	s_cselect_b64 s[60:61], -1, 0
	s_cbranch_vccz .LBB0_839
	v_max_f32_e32 v3, v3, v3
	v_max_f32_e32 v3, 0, v3
	v_exp_f32_e64 v16, -v3
	v_add_f32_e32 v249, v249, v3
	v_xor_b32_e32 v82, 0x80000000, v249
	v_mov_b32_e32 v83, v82
	v_mov_b32_e32 v84, v82
	v_mov_b32_e32 v85, v82
	v_mov_b32_e32 v86, v82
	v_mov_b32_e32 v87, v82
	v_mov_b32_e32 v88, v82
	v_mov_b32_e32 v89, v82
	v_mov_b32_e32 v90, v82
	v_mov_b32_e32 v91, v82
	v_mov_b32_e32 v92, v82
	v_mov_b32_e32 v93, v82
	v_mov_b32_e32 v94, v82
	v_mov_b32_e32 v95, v82
	v_mov_b32_e32 v96, v82
	v_mov_b32_e32 v97, v82
	s_and_saveexec_b64 s[64:65], s[24:25]
	ds_write_b32 v245, v16
	s_or_b64 exec, exec, s[64:65]
	v_sub_f32_e32 v129, v129, v3
	v_sub_f32_e32 v128, v128, v3
	v_sub_f32_e32 v127, v127, v3
	v_sub_f32_e32 v126, v126, v3
	v_sub_f32_e32 v125, v125, v3
	v_sub_f32_e32 v124, v124, v3
	v_sub_f32_e32 v123, v123, v3
	v_sub_f32_e32 v122, v122, v3
	v_sub_f32_e32 v121, v121, v3
	v_sub_f32_e32 v120, v120, v3
	v_sub_f32_e32 v119, v119, v3
	v_sub_f32_e32 v118, v118, v3
	v_sub_f32_e32 v117, v117, v3
	v_sub_f32_e32 v116, v116, v3
	v_sub_f32_e32 v115, v115, v3
	v_sub_f32_e32 v114, v114, v3
	v_sub_f32_e32 v113, v113, v3
	v_sub_f32_e32 v112, v112, v3
	v_sub_f32_e32 v111, v111, v3
	v_sub_f32_e32 v110, v110, v3
	v_sub_f32_e32 v109, v109, v3
	v_sub_f32_e32 v108, v108, v3
	v_sub_f32_e32 v107, v107, v3
	v_sub_f32_e32 v106, v106, v3
	v_sub_f32_e32 v105, v105, v3
	v_sub_f32_e32 v104, v104, v3
	v_sub_f32_e32 v103, v103, v3
	v_sub_f32_e32 v102, v102, v3
	v_sub_f32_e32 v101, v101, v3
	v_sub_f32_e32 v100, v100, v3
	v_sub_f32_e32 v99, v99, v3
	v_sub_f32_e32 v98, v98, v3
	v_mul_f32_e32 v246, v246, v16
	s_branch .LBB0_839

; #define LAS __attribute__((address_space(3)))
; #define SFENCE() __builtin_amdgcn_sched_barrier(0)
; #define CIPART(rel, g) do { const float mneg = (t0 + (rel) > tw_last) ? -INFINITY : -mhat; const LAS float* Gt = Gl + (rel) * 64 + 4 * hi + ((g) >> 2) * 32 + 8 * ((g) & 3); const f32x4 gg = *(const LAS f32x4*)Gt; \
;         _Pragma("unroll") for (int i = 0; i < 4; ++i) { if ((g) < 4) c0[4 * ((g) & 3) + i] = gg[i] + mneg; else c1[4 * ((g) & 3) + i] = gg[i] + mneg; } } while (0)
; template <bool FOX>
; __device__ __forceinline__ void attn_unit(const Args& A, int b, int h, int qb, LAS char* shm, LAS float* dg) {
;     ...
;         SFENCE();
;         { const lds_cptr kp = kp0 + ((t + 1) % NS) * KSLOT;
; #pragma unroll
;           for (int g = 0; g < 8; ++g) { const int i = (g >> 1) + 4 * (g & 1);
;               const bf16x8 vf = (bf16x8){vlo[i][0], vlo[i][1], vlo[i][2], vlo[i][3], vhi[i][0], vhi[i][1], vhi[i][2], vhi[i][3]};
;               o[g & 1] = __builtin_amdgcn_mfma_f32_32x32x16_bf16(__builtin_bit_cast(bf16x8, pw[g >> 1]), vf, o[g & 1], 0, 0, 0);
;               if (g < 4) {
; #pragma unroll
;                   for (int k = 0; k < 4; ++k) pp0[4 * g + k] = __builtin_amdgcn_exp2f(c0[4 * g + k]);
;                   asm volatile("" : "+v"(pp0)); }
;               else {
; #pragma unroll
;                   for (int k = 0; k < 4; ++k) pp1[4 * g - 16 + k] = __builtin_amdgcn_exp2f(c1[4 * g - 16 + k]);
;                   asm volatile("" : "+v"(pp1)); }
;               { constexpr int G0 = FOX ? 2 : 1; const int j = g - G0; if (j >= 0 && j < NQ) { kf[2 * j] = *(const LAS bf16x8*)(kp + j * 2048); kf[2 * j + 1] = *(const LAS bf16x8*)(kp + j * 2048 + 512); } }
;               if constexpr (FOX) { CIPART(t + 1, g); if (g < 4) asm volatile("" : "+v"(c0)); else asm volatile("" : "+v"(c1)); }
;               SFENCE();
;           } }
;         if (resc) { asm volatile("s_waitcnt lgkmcnt(0)" ::: "memory");
; #pragma unroll
;             for (int rq = 0; rq < 4; ++rq) { const f32x4 af = *(const LAS f32x4*)(wsf + 8 * rq + 4 * hi);
; #pragma unroll
;                 for (int i = 0; i < 4; ++i) { o[0][4 * rq + i] *= af[i]; o[1][4 * rq + i] *= af[i]; } } }
.Lmla_mid_skip:
	s_waitcnt lgkmcnt(0)
	v_mfma_f32_32x32x16_bf16 v[18:33], v[186:189], v[206:209], v[18:33]
	s_add_i32 s27, s26, 1
	s_and_b32 s64, s27, 3
	s_mulk_i32 s64, 0x3000
	v_exp_f32_e32 v66, v114
	v_exp_f32_e32 v67, v115
	v_exp_f32_e32 v68, v116
	v_exp_f32_e32 v69, v117
	v_add_u32_e32 v3, s64, v248
	v_mfma_f32_32x32x16_bf16 v[34:49], v[186:189], v[194:197], v[34:49]
	v_exp_f32_e32 v70, v118
	v_exp_f32_e32 v71, v119
	v_exp_f32_e32 v72, v120
	v_exp_f32_e32 v73, v121
	ds_read_b128 v[206:209], v3
	ds_read_b128 v[194:197], v3 offset:512
	v_mfma_f32_32x32x16_bf16 v[18:33], v[182:185], v[202:205], v[18:33]
	v_exp_f32_e32 v74, v122
	v_exp_f32_e32 v75, v123
	v_exp_f32_e32 v76, v124
	v_exp_f32_e32 v77, v125
	ds_read_b128 v[202:205], v3 offset:2048
	ds_read_b128 v[186:189], v3 offset:2560
	v_mfma_f32_32x32x16_bf16 v[34:49], v[182:185], v[214:217], v[34:49]
	v_exp_f32_e32 v78, v126
	v_exp_f32_e32 v79, v127
	v_exp_f32_e32 v80, v128
	v_exp_f32_e32 v81, v129
	ds_read_b128 v[198:201], v3 offset:4096
	ds_read_b128 v[182:185], v3 offset:4608
	v_mfma_f32_32x32x16_bf16 v[18:33], v[178:181], v[210:213], v[18:33]
	v_exp_f32_e32 v50, v98
	v_exp_f32_e32 v51, v99
	v_exp_f32_e32 v52, v100
	v_exp_f32_e32 v53, v101
	ds_read_b128 v[190:193], v3 offset:6144
	ds_read_b128 v[170:173], v3 offset:6656
	v_mfma_f32_32x32x16_bf16 v[34:49], v[178:181], v[12:15], v[34:49]
	v_exp_f32_e32 v54, v102
	v_exp_f32_e32 v55, v103
	v_exp_f32_e32 v56, v104
	v_exp_f32_e32 v57, v105
	ds_read_b128 v[178:181], v3 offset:8192
	ds_read_b128 v[166:169], v3 offset:8704
	v_mfma_f32_32x32x16_bf16 v[18:33], v[218:221], v[8:11], v[18:33]
	v_exp_f32_e32 v58, v106
	v_exp_f32_e32 v59, v107
	v_exp_f32_e32 v60, v108
	v_exp_f32_e32 v61, v109
	ds_read_b128 v[174:177], v3 offset:10240
	ds_read_b128 v[162:165], v3 offset:10752
	v_mfma_f32_32x32x16_bf16 v[34:49], v[218:221], v[4:7], v[34:49]
	v_exp_f32_e32 v62, v110
	v_exp_f32_e32 v63, v111
	v_exp_f32_e32 v64, v112
	v_exp_f32_e32 v65, v113
	s_andn2_b64 vcc, exec, s[60:61]
	s_cbranch_vccnz .LBB0_841
	s_waitcnt lgkmcnt(0)
	ds_read_b128 v[4:7], v244 offset:96
	ds_read_b128 v[8:11], v244 offset:64
	ds_read_b128 v[12:15], v244 offset:32
	ds_read_b128 v[98:101], v244
	s_waitcnt lgkmcnt(3)
	v_pk_mul_f32 v[32:33], v[32:33], v[6:7]
	s_waitcnt lgkmcnt(2)
	v_pk_mul_f32 v[28:29], v[28:29], v[10:11]
	s_waitcnt lgkmcnt(1)
	v_pk_mul_f32 v[24:25], v[24:25], v[14:15]
	s_waitcnt lgkmcnt(0)
	v_pk_mul_f32 v[20:21], v[20:21], v[100:101]
	v_pk_mul_f32 v[30:31], v[30:31], v[4:5]
	v_pk_mul_f32 v[26:27], v[26:27], v[8:9]
	v_pk_mul_f32 v[22:23], v[22:23], v[12:13]
	v_pk_mul_f32 v[18:19], v[18:19], v[98:99]
	v_pk_mul_f32 v[48:49], v[48:49], v[6:7]
	v_pk_mul_f32 v[44:45], v[44:45], v[10:11]
	v_pk_mul_f32 v[40:41], v[40:41], v[14:15]
	v_pk_mul_f32 v[36:37], v[36:37], v[100:101]
	v_pk_mul_f32 v[46:47], v[46:47], v[4:5]
	v_pk_mul_f32 v[42:43], v[42:43], v[8:9]
	v_pk_mul_f32 v[38:39], v[38:39], v[12:13]
	v_pk_mul_f32 v[34:35], v[34:35], v[98:99]

; #define WAITV(n) do { switch (n) { WV_(0) WV_(1) WV_(2) WV_(3) WV_(4) WV_(5) default: asm volatile("s_waitcnt vmcnt(6)" ::: "memory"); break; } } while (0)
; #define LBAR() asm volatile("s_waitcnt lgkmcnt(0)\n\ts_barrier" ::: "memory")
; template <bool FOX>
; __device__ __forceinline__ void attn_unit(const Args& A, int b, int h, int qb, LAS char* shm, LAS float* dg) {
;     ...
;         WAITV(((t + 3 < nti ? nK : 0) + (t + 1 < nti ? 1 : 0)) + ((t + 4 < nti ? nK : 0) + (t + 2 < nti ? 1 : 0)));
;         LBAR();
;     }
.LBB0_864:
	s_waitcnt lgkmcnt(0)
	s_barrier
	s_branch .Lmla_after_bar
.Lmla_g2_end:
	s_waitcnt lgkmcnt(0)
.Lmla_after_bar:
	s_add_u32 s42, s42, 0x2000
	s_addc_u32 s43, s43, 0
	s_cmp_eq_u32 s27, s96
	v_lshl_add_u64 v[234:235], v[234:235], 0, s[62:63]
	s_cbranch_scc1 .LBB0_867
	s_mov_b32 s26, s27
	s_branch .LBB0_825
